# speedup vs baseline: 1.0052x; 1.0005x over previous
.LBB2_11:
	s_or_b64 exec, exec, s[8:9]
	v_or_b32_e32 v1, 31, v1
	v_min_i32_e32 v2, 0x247, v1
	v_add_u32_e32 v2, 64, v2
	v_ashrrev_i32_e32 v2, 6, v2
	v_cmp_lt_i32_e32 vcc, s18, v1
	s_nop 1
	v_cndmask_b32_e32 v85, 9, v2, vcc
	v_readfirstlane_b32 s28, v97
	s_cmp_lt_u32 s28, 16
	s_cselect_b32 s29, 1, 0
	s_cmp_eq_u32 s28, 18
	s_cselect_b32 s28, 1, 0
	s_or_b32 s29, s29, s28
	v_subrev_u32_e32 v85, s29, v85
	v_cmp_lt_i32_e32 vcc, 0, v85
	s_nop 0
	s_and_saveexec_b64 s[8:9], vcc
	s_cbranch_execz .LBB2_23
	v_max_i32_e32 v98, 0x205, v3
	v_mov_b32_e32 v1, 0
	v_mov_b64_e32 v[2:3], v[0:1]
	v_mov_b64_e32 v[4:5], v[0:1]
	v_mov_b64_e32 v[6:7], v[0:1]
	v_mov_b64_e32 v[8:9], v[0:1]
	v_mov_b64_e32 v[10:11], v[0:1]
	v_mov_b64_e32 v[12:13], v[0:1]
	v_mov_b64_e32 v[14:15], v[0:1]
	v_mov_b64_e32 v[16:17], v[0:1]
	v_mov_b64_e32 v[18:19], v[0:1]
	v_mov_b64_e32 v[20:21], v[0:1]
	v_mov_b64_e32 v[22:23], v[0:1]
	v_mov_b64_e32 v[24:25], v[0:1]
	v_mov_b64_e32 v[26:27], v[0:1]
	v_mov_b64_e32 v[28:29], v[0:1]
	v_mov_b64_e32 v[30:31], v[0:1]
	v_mov_b64_e32 v[32:33], v[0:1]
	s_mov_b32 s21, 0
	v_mov_b32_e32 v104, 0
	s_mov_b32 s31, 0
	s_mov_b64 s[10:11], 0
	v_mov_b32_e32 v99, v88
	v_mov_b32_e32 v100, v89
	v_mov_b32_e32 v101, v90
	v_mov_b32_e32 v102, v91
	v_mov_b32_e32 v103, v93
	v_readfirstlane_b32 s30, v85
	v_mov_b32_e32 v117, v114
	v_mov_b32_e32 v118, v115
	v_mov_b32_e32 v119, v116
	s_branch .LBB2_14
